# baseline (speedup 1.0000x reference)
.Lw_ld_done:
	s_waitcnt vmcnt(60)
	v_and_b32_e32 v242, 0xffff0000, v3
	v_lshlrev_b32_e32 v240, 3, v0
	v_sub_f32_e32 v244, v3, v242
	v_and_b32_e32 v242, 0xffff0000, v4
	v_and_b32_e32 v148, 0xf8, v240
	v_and_b32_e32 v240, 0xffff0000, v2
	v_sub_f32_e32 v245, v4, v242
	v_and_b32_e32 v242, 0xffff0000, v5
	v_sub_f32_e32 v240, v2, v240
	v_sub_f32_e32 v246, v5, v242
	v_mad_u32_u24 v247, v1, s17, v148
	v_perm_b32 v242, v3, v2, s14
	v_perm_b32 v243, v5, v4, s14
	ds_write_b64 v247, v[242:243]
	v_perm_b32 v242, v244, v240, s14
	v_perm_b32 v243, v246, v245, s14
	ds_write_b64 v247, v[242:243] offset:13056
	v_and_b32_e32 v242, 0xffff0000, v7
	v_sub_f32_e32 v244, v7, v242
	v_and_b32_e32 v242, 0xffff0000, v8
	v_and_b32_e32 v240, 0xffff0000, v6
	v_sub_f32_e32 v245, v8, v242
	v_and_b32_e32 v242, 0xffff0000, v9
	v_sub_f32_e32 v240, v6, v240
	v_sub_f32_e32 v246, v9, v242
	v_mad_u32_u24 v241, v146, s17, v148
	v_perm_b32 v242, v7, v6, s14
	v_perm_b32 v243, v9, v8, s14
	ds_write_b64 v241, v[242:243]
	v_perm_b32 v242, v244, v240, s14
	v_perm_b32 v243, v246, v245, s14
	ds_write_b64 v241, v[242:243] offset:13056
	v_and_b32_e32 v242, 0xffff0000, v11
	v_sub_f32_e32 v244, v11, v242
	v_and_b32_e32 v242, 0xffff0000, v12
	v_and_b32_e32 v240, 0xffff0000, v10
	v_sub_f32_e32 v245, v12, v242
	v_and_b32_e32 v242, 0xffff0000, v13
	v_sub_f32_e32 v240, v10, v240
	v_sub_f32_e32 v246, v13, v242
	v_perm_b32 v242, v11, v10, s14
	v_perm_b32 v243, v13, v12, s14
	ds_write_b64 v247, v[242:243] offset:8704
	v_perm_b32 v242, v244, v240, s14
	v_perm_b32 v243, v246, v245, s14
	ds_write_b64 v247, v[242:243] offset:21760
	s_waitcnt vmcnt(0)
	v_cvt_pk_bf16_f32 v106, v112, v113
	v_lshlrev_b32_e32 v248, 16, v106
	v_and_b32_e32 v249, 0xffff0000, v106
	v_sub_f32_e32 v248, v112, v248
	v_sub_f32_e32 v249, v113, v249
	v_cvt_pk_bf16_f32 v102, v248, v249
	v_cvt_pk_bf16_f32 v107, v114, v115
	v_lshlrev_b32_e32 v250, 16, v107
	v_and_b32_e32 v251, 0xffff0000, v107
	v_sub_f32_e32 v250, v114, v250
	v_sub_f32_e32 v251, v115, v251
	v_cvt_pk_bf16_f32 v103, v250, v251
	v_cvt_pk_bf16_f32 v108, v116, v117
	v_lshlrev_b32_e32 v248, 16, v108
	v_and_b32_e32 v249, 0xffff0000, v108
	v_sub_f32_e32 v248, v116, v248
	v_sub_f32_e32 v249, v117, v249
	v_cvt_pk_bf16_f32 v104, v248, v249
	v_cvt_pk_bf16_f32 v109, v118, v119
	v_lshlrev_b32_e32 v250, 16, v109
	v_and_b32_e32 v251, 0xffff0000, v109
	v_sub_f32_e32 v250, v118, v250
	v_sub_f32_e32 v251, v119, v251
	v_cvt_pk_bf16_f32 v105, v250, v251
	v_cvt_pk_bf16_f32 v74, v176, v178
	v_lshlrev_b32_e32 v248, 16, v74
	v_and_b32_e32 v249, 0xffff0000, v74
	v_sub_f32_e32 v248, v176, v248
	v_sub_f32_e32 v249, v178, v249
	v_cvt_pk_bf16_f32 v70, v248, v249
	v_cvt_pk_bf16_f32 v75, v180, v182
	v_lshlrev_b32_e32 v250, 16, v75
	v_and_b32_e32 v251, 0xffff0000, v75
	v_sub_f32_e32 v250, v180, v250
	v_sub_f32_e32 v251, v182, v251
	v_cvt_pk_bf16_f32 v71, v250, v251
	v_cvt_pk_bf16_f32 v76, v184, v186
	v_lshlrev_b32_e32 v248, 16, v76
	v_and_b32_e32 v249, 0xffff0000, v76
	v_sub_f32_e32 v248, v184, v248
	v_sub_f32_e32 v249, v186, v249
	v_cvt_pk_bf16_f32 v72, v248, v249
	v_cvt_pk_bf16_f32 v77, v188, v190
	v_lshlrev_b32_e32 v250, 16, v77
	v_and_b32_e32 v251, 0xffff0000, v77
	v_sub_f32_e32 v250, v188, v250
	v_sub_f32_e32 v251, v190, v251
	v_cvt_pk_bf16_f32 v73, v250, v251
	v_cvt_pk_bf16_f32 v38, v177, v179
	v_lshlrev_b32_e32 v248, 16, v38
	v_and_b32_e32 v249, 0xffff0000, v38
	v_sub_f32_e32 v248, v177, v248
	v_sub_f32_e32 v249, v179, v249
	v_cvt_pk_bf16_f32 v42, v248, v249
	v_cvt_pk_bf16_f32 v39, v181, v183
	v_lshlrev_b32_e32 v250, 16, v39
	v_and_b32_e32 v251, 0xffff0000, v39
	v_sub_f32_e32 v250, v181, v250
	v_sub_f32_e32 v251, v183, v251
	v_cvt_pk_bf16_f32 v43, v250, v251
	v_cvt_pk_bf16_f32 v40, v185, v187
	v_lshlrev_b32_e32 v248, 16, v40
	v_and_b32_e32 v249, 0xffff0000, v40
	v_sub_f32_e32 v248, v185, v248
	v_sub_f32_e32 v249, v187, v249
	v_cvt_pk_bf16_f32 v44, v248, v249
	v_cvt_pk_bf16_f32 v41, v189, v191
	v_lshlrev_b32_e32 v250, 16, v41
	v_and_b32_e32 v251, 0xffff0000, v41
	v_sub_f32_e32 v250, v189, v250
	v_sub_f32_e32 v251, v191, v251
	v_cvt_pk_bf16_f32 v45, v250, v251
	v_cvt_pk_bf16_f32 v98, v120, v121
	v_lshlrev_b32_e32 v248, 16, v98
	v_and_b32_e32 v249, 0xffff0000, v98
	v_sub_f32_e32 v248, v120, v248
	v_sub_f32_e32 v249, v121, v249
	v_cvt_pk_bf16_f32 v94, v248, v249
	v_cvt_pk_bf16_f32 v99, v122, v123
	v_lshlrev_b32_e32 v250, 16, v99
	v_and_b32_e32 v251, 0xffff0000, v99
	v_sub_f32_e32 v250, v122, v250
	v_sub_f32_e32 v251, v123, v251
	v_cvt_pk_bf16_f32 v95, v250, v251
	v_cvt_pk_bf16_f32 v100, v124, v125
	v_lshlrev_b32_e32 v248, 16, v100
	v_and_b32_e32 v249, 0xffff0000, v100
	v_sub_f32_e32 v248, v124, v248
	v_sub_f32_e32 v249, v125, v249
	v_cvt_pk_bf16_f32 v96, v248, v249
	v_cvt_pk_bf16_f32 v101, v126, v127
	v_lshlrev_b32_e32 v250, 16, v101
	v_and_b32_e32 v251, 0xffff0000, v101
	v_sub_f32_e32 v250, v126, v250
	v_sub_f32_e32 v251, v127, v251
	v_cvt_pk_bf16_f32 v97, v250, v251
	v_cvt_pk_bf16_f32 v62, v192, v194
	v_lshlrev_b32_e32 v248, 16, v62
	v_and_b32_e32 v249, 0xffff0000, v62
	v_sub_f32_e32 v248, v192, v248
	v_sub_f32_e32 v249, v194, v249
	v_cvt_pk_bf16_f32 v66, v248, v249
	v_cvt_pk_bf16_f32 v63, v196, v198
	v_lshlrev_b32_e32 v250, 16, v63
	v_and_b32_e32 v251, 0xffff0000, v63
	v_sub_f32_e32 v250, v196, v250
	v_sub_f32_e32 v251, v198, v251
	v_cvt_pk_bf16_f32 v67, v250, v251
	v_cvt_pk_bf16_f32 v64, v200, v202
	v_lshlrev_b32_e32 v248, 16, v64
	v_and_b32_e32 v249, 0xffff0000, v64
	v_sub_f32_e32 v248, v200, v248
	v_sub_f32_e32 v249, v202, v249
	v_cvt_pk_bf16_f32 v68, v248, v249
	v_cvt_pk_bf16_f32 v65, v204, v206
	v_lshlrev_b32_e32 v250, 16, v65
	v_and_b32_e32 v251, 0xffff0000, v65
	v_sub_f32_e32 v250, v204, v250
	v_sub_f32_e32 v251, v206, v251
	v_cvt_pk_bf16_f32 v69, v250, v251
	v_cvt_pk_bf16_f32 v30, v193, v195
	v_lshlrev_b32_e32 v248, 16, v30
	v_and_b32_e32 v249, 0xffff0000, v30
	v_sub_f32_e32 v248, v193, v248
	v_sub_f32_e32 v249, v195, v249
	v_cvt_pk_bf16_f32 v34, v248, v249
	v_cvt_pk_bf16_f32 v31, v197, v199
	v_lshlrev_b32_e32 v250, 16, v31
	v_and_b32_e32 v251, 0xffff0000, v31
	v_sub_f32_e32 v250, v197, v250
	v_sub_f32_e32 v251, v199, v251
	v_cvt_pk_bf16_f32 v35, v250, v251
	v_cvt_pk_bf16_f32 v32, v201, v203
	v_lshlrev_b32_e32 v248, 16, v32
	v_and_b32_e32 v249, 0xffff0000, v32
	v_sub_f32_e32 v248, v201, v248
	v_sub_f32_e32 v249, v203, v249
	v_cvt_pk_bf16_f32 v36, v248, v249
	v_cvt_pk_bf16_f32 v33, v205, v207
	v_lshlrev_b32_e32 v250, 16, v33
	v_and_b32_e32 v251, 0xffff0000, v33
	v_sub_f32_e32 v250, v205, v250
	v_sub_f32_e32 v251, v207, v251
	v_cvt_pk_bf16_f32 v37, v250, v251
	v_cvt_pk_bf16_f32 v90, v128, v129
	v_lshlrev_b32_e32 v248, 16, v90
	v_and_b32_e32 v249, 0xffff0000, v90
	v_sub_f32_e32 v248, v128, v248
	v_sub_f32_e32 v249, v129, v249
	v_cvt_pk_bf16_f32 v86, v248, v249
	v_cvt_pk_bf16_f32 v91, v130, v131
	v_lshlrev_b32_e32 v250, 16, v91
	v_and_b32_e32 v251, 0xffff0000, v91
	v_sub_f32_e32 v250, v130, v250
	v_sub_f32_e32 v251, v131, v251
	v_cvt_pk_bf16_f32 v87, v250, v251
	v_cvt_pk_bf16_f32 v92, v132, v133
	v_lshlrev_b32_e32 v248, 16, v92
	v_and_b32_e32 v249, 0xffff0000, v92
	v_sub_f32_e32 v248, v132, v248
	v_sub_f32_e32 v249, v133, v249
	v_cvt_pk_bf16_f32 v88, v248, v249
	v_cvt_pk_bf16_f32 v93, v134, v135
	v_lshlrev_b32_e32 v250, 16, v93
	v_and_b32_e32 v251, 0xffff0000, v93
	v_sub_f32_e32 v250, v134, v250
	v_sub_f32_e32 v251, v135, v251
	v_cvt_pk_bf16_f32 v89, v250, v251
	v_cvt_pk_bf16_f32 v54, v208, v210
	v_lshlrev_b32_e32 v248, 16, v54
	v_and_b32_e32 v249, 0xffff0000, v54
	v_sub_f32_e32 v248, v208, v248
	v_sub_f32_e32 v249, v210, v249
	v_cvt_pk_bf16_f32 v58, v248, v249
	v_cvt_pk_bf16_f32 v55, v212, v214
	v_lshlrev_b32_e32 v250, 16, v55
	v_and_b32_e32 v251, 0xffff0000, v55
	v_sub_f32_e32 v250, v212, v250
	v_sub_f32_e32 v251, v214, v251
	v_cvt_pk_bf16_f32 v59, v250, v251
	v_cvt_pk_bf16_f32 v56, v216, v218
	v_lshlrev_b32_e32 v248, 16, v56
	v_and_b32_e32 v249, 0xffff0000, v56
	v_sub_f32_e32 v248, v216, v248
	v_sub_f32_e32 v249, v218, v249
	v_cvt_pk_bf16_f32 v60, v248, v249
	v_cvt_pk_bf16_f32 v57, v220, v222
	v_lshlrev_b32_e32 v250, 16, v57
	v_and_b32_e32 v251, 0xffff0000, v57
	v_sub_f32_e32 v250, v220, v250
	v_sub_f32_e32 v251, v222, v251
	v_cvt_pk_bf16_f32 v61, v250, v251
	v_cvt_pk_bf16_f32 v26, v209, v211
	v_lshlrev_b32_e32 v248, 16, v26
	v_and_b32_e32 v249, 0xffff0000, v26
	v_sub_f32_e32 v248, v209, v248
	v_sub_f32_e32 v249, v211, v249
	v_cvt_pk_bf16_f32 v22, v248, v249
	v_cvt_pk_bf16_f32 v27, v213, v215
	v_lshlrev_b32_e32 v250, 16, v27
	v_and_b32_e32 v251, 0xffff0000, v27
	v_sub_f32_e32 v250, v213, v250
	v_sub_f32_e32 v251, v215, v251
	v_cvt_pk_bf16_f32 v23, v250, v251
	v_cvt_pk_bf16_f32 v28, v217, v219
	v_lshlrev_b32_e32 v248, 16, v28
	v_and_b32_e32 v249, 0xffff0000, v28
	v_sub_f32_e32 v248, v217, v248
	v_sub_f32_e32 v249, v219, v249
	v_cvt_pk_bf16_f32 v24, v248, v249
	v_cvt_pk_bf16_f32 v29, v221, v223
	v_lshlrev_b32_e32 v250, 16, v29
	v_and_b32_e32 v251, 0xffff0000, v29
	v_sub_f32_e32 v250, v221, v250
	v_sub_f32_e32 v251, v223, v251
	v_cvt_pk_bf16_f32 v25, v250, v251
	v_cvt_pk_bf16_f32 v82, v136, v137
	v_lshlrev_b32_e32 v248, 16, v82
	v_and_b32_e32 v249, 0xffff0000, v82
	v_sub_f32_e32 v248, v136, v248
	v_sub_f32_e32 v249, v137, v249
	v_cvt_pk_bf16_f32 v78, v248, v249
	v_cvt_pk_bf16_f32 v83, v138, v139
	v_lshlrev_b32_e32 v250, 16, v83
	v_and_b32_e32 v251, 0xffff0000, v83
	v_sub_f32_e32 v250, v138, v250
	v_sub_f32_e32 v251, v139, v251
	v_cvt_pk_bf16_f32 v79, v250, v251
	v_cvt_pk_bf16_f32 v84, v140, v141
	v_lshlrev_b32_e32 v248, 16, v84
	v_and_b32_e32 v249, 0xffff0000, v84
	v_sub_f32_e32 v248, v140, v248
	v_sub_f32_e32 v249, v141, v249
	v_cvt_pk_bf16_f32 v80, v248, v249
	v_cvt_pk_bf16_f32 v85, v142, v143
	v_lshlrev_b32_e32 v250, 16, v85
	v_and_b32_e32 v251, 0xffff0000, v85
	v_sub_f32_e32 v250, v142, v250
	v_sub_f32_e32 v251, v143, v251
	v_cvt_pk_bf16_f32 v81, v250, v251
	v_cvt_pk_bf16_f32 v46, v224, v226
	v_lshlrev_b32_e32 v248, 16, v46
	v_and_b32_e32 v249, 0xffff0000, v46
	v_sub_f32_e32 v248, v224, v248
	v_sub_f32_e32 v249, v226, v249
	v_cvt_pk_bf16_f32 v50, v248, v249
	v_cvt_pk_bf16_f32 v47, v228, v230
	v_lshlrev_b32_e32 v250, 16, v47
	v_and_b32_e32 v251, 0xffff0000, v47
	v_sub_f32_e32 v250, v228, v250
	v_sub_f32_e32 v251, v230, v251
	v_cvt_pk_bf16_f32 v51, v250, v251
	v_cvt_pk_bf16_f32 v48, v232, v234
	v_lshlrev_b32_e32 v248, 16, v48
	v_and_b32_e32 v249, 0xffff0000, v48
	v_sub_f32_e32 v248, v232, v248
	v_sub_f32_e32 v249, v234, v249
	v_cvt_pk_bf16_f32 v52, v248, v249
	v_cvt_pk_bf16_f32 v49, v236, v238
	v_lshlrev_b32_e32 v250, 16, v49
	v_and_b32_e32 v251, 0xffff0000, v49
	v_sub_f32_e32 v250, v236, v250
	v_sub_f32_e32 v251, v238, v251
	v_cvt_pk_bf16_f32 v53, v250, v251
	v_cvt_pk_bf16_f32 v18, v225, v227
	v_lshlrev_b32_e32 v248, 16, v18
	v_and_b32_e32 v249, 0xffff0000, v18
	v_sub_f32_e32 v248, v225, v248
	v_sub_f32_e32 v249, v227, v249
	v_cvt_pk_bf16_f32 v14, v248, v249
	v_cvt_pk_bf16_f32 v19, v229, v231
	v_lshlrev_b32_e32 v250, 16, v19
	v_and_b32_e32 v251, 0xffff0000, v19
	v_sub_f32_e32 v250, v229, v250
	v_sub_f32_e32 v251, v231, v251
	v_cvt_pk_bf16_f32 v15, v250, v251
	v_cvt_pk_bf16_f32 v20, v233, v235
	v_lshlrev_b32_e32 v248, 16, v20
	v_and_b32_e32 v249, 0xffff0000, v20
	v_sub_f32_e32 v248, v233, v248
	v_sub_f32_e32 v249, v235, v249
	v_cvt_pk_bf16_f32 v16, v248, v249
	v_cvt_pk_bf16_f32 v21, v237, v239
	v_lshlrev_b32_e32 v250, 16, v21
	v_and_b32_e32 v251, 0xffff0000, v21
	v_sub_f32_e32 v250, v237, v250
	v_sub_f32_e32 v251, v239, v251
	v_cvt_pk_bf16_f32 v17, v250, v251
	v_mov_b32_e32 v113, 0
	v_cmp_gt_u32_e32 vcc, 0x100, v0
	v_and_b32_e32 v115, 63, v0
	v_lshrrev_b32_e32 v125, 2, v115
	v_lshlrev_b32_e32 v114, 2, v0
	v_and_b32_e32 v114, 12, v114
	v_mul_u32_u24_e32 v115, 20, v125
	v_mul_u32_u24_e32 v112, 0xa00, v149
	v_lshlrev_b32_e32 v115, 2, v115
	v_lshlrev_b32_e32 v120, 2, v114
	v_add3_u32 v118, v112, v115, v120
	v_lshlrev_b32_e32 v112, 2, v151
	v_lshl_add_u64 v[114:115], s[26:27], 0, v[112:113]
	v_mov_b32_e32 v112, 0x100
	v_cndmask_b32_e64 v112, v112, 0, vcc
	v_lshl_add_u64 v[122:123], s[28:29], 0, v[112:113]
	v_lshlrev_b32_e32 v112, 1, v153
	v_mov_b32_e32 v121, v113
	v_lshl_add_u64 v[112:113], v[122:123], 0, v[112:113]
	v_lshl_add_u64 v[114:115], v[114:115], 0, v[120:121]
	v_lshl_add_u64 v[112:113], v[112:113], 0, v[120:121]
	v_mul_u32_u24_e32 v120, 0x50, v152
	v_or_b32_e32 v120, v120, v150
	v_and_b32_e32 v124, 48, v0
	s_movk_i32 s4, 0xa00
	v_lshlrev_b32_e32 v120, 2, v120
	v_add_u32_e32 v122, s15, v125
	v_mul_u32_u24_e32 v116, 0x110, v1
	v_mul_u32_u24_e32 v117, 0x110, v146
	v_or_b32_e32 v119, 0xc350, v125
	s_max_u32 s6, s10, 1
	v_mad_u32_u24 v120, v149, s4, v120
	v_mad_u32_u24 v121, v150, s17, v124
	v_add_u32_e32 v122, 0xffffd887, v122
	v_add_u32_e32 v240, 0xcc00, v120
	v_add_u32_e32 v241, 0xd000, v120
	v_mov_b32_e32 v242, v119
	v_mov_b32_e32 v243, 0
	v_lshlrev_b64 v[244:245], 9, v[242:243]
	v_lshl_add_u64 v[228:229], v[114:115], 0, v[244:245]
	v_lshl_add_u64 v[230:231], v[112:113], 0, v[244:245]
	s_waitcnt lgkmcnt(0)
	s_barrier
	s_branch .LBB0_9
